# speedup vs baseline: 1.6872x; 1.0134x over previous
.LBB1_31:
	s_waitcnt vmcnt(6)
	v_mbcnt_lo_u32_b32 v64, -1, 0
	v_mbcnt_hi_u32_b32 v100, -1, v64
	s_andn2_b32 s25, s25, 63
	v_add_u32_e32 v64, s25, v100
	v_ashrrev_i32_e32 v64, 4, v64
	s_movk_i32 s0, 0x44
	v_and_b32_e32 v101, 15, v100
	v_mul_lo_u32 v64, v64, s0
	v_lshl_add_u32 v64, v101, 2, v64
	s_and_b64 vcc, exec, s[8:9]
	s_barrier
	ds_write_b32 v64, v104
	ds_write_b32 v64, v105 offset:1360
	ds_write_b32 v64, v106 offset:2720
	ds_write_b32 v64, v107 offset:4080
	s_waitcnt lgkmcnt(0)
	s_barrier
	s_cbranch_vccz .LBB1_38
	v_and_b32_e32 v64, 3, v100
	v_and_b32_e32 v65, 0x7c, v100
	s_movk_i32 s0, 0x550
	v_mad_u32_u24 v70, v64, s0, v65
	ds_read2_b32 v[64:65], v70 offset1:17
	ds_read2_b32 v[66:67], v70 offset0:34 offset1:51
	ds_read2_b32 v[68:69], v70 offset0:68 offset1:85
	s_mov_b32 s0, 0xf800000
	s_lshl_b32 s10, s23, 8
	s_waitcnt lgkmcnt(2)
	v_add_f32_e32 v64, 0, v64
	v_add_f32_e32 v64, v64, v65
	s_waitcnt lgkmcnt(1)
	v_add_f32_e32 v66, v64, v66
	ds_read2_b32 v[64:65], v70 offset0:102 offset1:119
	v_add_f32_e32 v66, v66, v67
	s_waitcnt lgkmcnt(1)
	v_add_f32_e32 v66, v66, v68
	v_add_f32_e32 v68, v66, v69
	ds_read2_b32 v[66:67], v70 offset0:136 offset1:153
	s_waitcnt lgkmcnt(1)
	v_add_f32_e32 v64, v68, v64
	ds_read2_b32 v[68:69], v70 offset0:170 offset1:187
	v_add_f32_e32 v71, v64, v65
	ds_read2_b32 v[64:65], v70 offset0:204 offset1:221
	s_waitcnt lgkmcnt(2)
	v_add_f32_e32 v66, v71, v66
	v_add_f32_e32 v66, v66, v67
	s_waitcnt lgkmcnt(1)
	v_add_f32_e32 v66, v66, v68
	v_add_f32_e32 v66, v66, v69
	s_waitcnt lgkmcnt(0)
	v_add_f32_e32 v64, v66, v64
	ds_read2_b32 v[66:67], v70 offset0:238 offset1:255
	v_add_u32_e32 v70, 0x400, v70
	ds_read2_b32 v[68:69], v70 offset0:16 offset1:33
	v_add_f32_e32 v71, v64, v65
	ds_read2_b32 v[64:65], v70 offset0:50 offset1:67
	s_waitcnt lgkmcnt(2)
	v_add_f32_e32 v66, v71, v66
	v_add_f32_e32 v66, v66, v67
	s_waitcnt lgkmcnt(1)
	v_add_f32_e32 v66, v66, v68
	v_add_f32_e32 v66, v66, v69
	s_waitcnt lgkmcnt(0)
	v_add_f32_e32 v64, v66, v64
	v_add_f32_e32 v64, v64, v65
	v_mul_f32_e32 v65, 0x4f800000, v64
	v_cmp_gt_f32_e32 vcc, s0, v64
	v_mov_b32_e32 v70, v58
	v_mov_b32_e32 v71, v50
	v_cndmask_b32_e32 v64, v64, v65, vcc
	v_sqrt_f32_e32 v65, v64
	s_waitcnt vmcnt(0)
	s_mul_i32 s16, s24, 0x1400
	s_add_u32 s16, s6, s16
	s_addc_u32 s17, s7, 0
	s_add_u32 s18, s16, 0x1000
	s_addc_u32 s19, s17, 0
	v_lshlrev_b32_e32 v122, 2, v100
	global_load_dword v103, v122, s[16:17]
	global_load_dword v104, v122, s[16:17] offset:256
	global_load_dword v105, v122, s[16:17] offset:512
	global_load_dword v106, v122, s[16:17] offset:768
	global_load_dword v107, v122, s[16:17] offset:1024
	global_load_dword v108, v122, s[16:17] offset:1280
	global_load_dword v109, v122, s[16:17] offset:1536
	global_load_dword v110, v122, s[16:17] offset:1792
	global_load_dword v111, v122, s[16:17] offset:2048
	global_load_dword v112, v122, s[16:17] offset:2304
	global_load_dword v113, v122, s[16:17] offset:2560
	global_load_dword v114, v122, s[16:17] offset:2816
	global_load_dword v115, v122, s[16:17] offset:3072
	global_load_dword v116, v122, s[16:17] offset:3328
	global_load_dword v117, v122, s[16:17] offset:3584
	global_load_dword v118, v122, s[16:17] offset:3840
	global_load_dword v119, v122, s[18:19]
	global_load_dword v120, v122, s[18:19] offset:256
	global_load_dword v121, v122, s[18:19] offset:512
	global_load_dword v122, v122, s[18:19] offset:768
	v_mov_b32_e32 v72, v59
	v_mov_b32_e32 v73, v51
	v_mov_b32_e32 v74, v41
	v_add_u32_e32 v66, -1, v65
	v_fma_f32 v67, -v66, v65, v64
	v_cmp_ge_f32_e64 s[0:1], 0, v67
	v_add_u32_e32 v67, 1, v65
	v_mov_b32_e32 v75, v33
	v_cndmask_b32_e64 v66, v65, v66, s[0:1]
	v_fma_f32 v65, -v67, v65, v64
	v_cmp_lt_f32_e64 s[0:1], 0, v65
	v_mov_b32_e32 v76, v43
	v_mov_b32_e32 v77, v35
	v_cndmask_b32_e64 v65, v66, v67, s[0:1]
	v_mul_f32_e32 v66, 0x37800000, v65
	v_cndmask_b32_e32 v65, v65, v66, vcc
	v_mov_b32_e32 v66, 0x260
	v_cmp_class_f32_e32 vcc, v64, v66
	v_mov_b32_e32 v78, v25
	v_mov_b32_e32 v79, v17
	v_cndmask_b32_e32 v64, v65, v64, vcc
	v_add_f32_e32 v64, 0x322bcc77, v64
	v_div_scale_f32 v65, s[0:1], v64, v64, 1.0
	v_rcp_f32_e32 v66, v65
	s_mul_i32 s0, s23, 0x180
	s_add_i32 s8, s10, s0
	s_mov_b32 s0, 0x3a83126f
	v_fma_f32 v67, -v65, v66, 1.0
	v_fmac_f32_e32 v66, v67, v66
	v_div_scale_f32 v67, vcc, 1.0, v64, 1.0
	v_mul_f32_e32 v68, v67, v66
	v_fma_f32 v69, -v65, v68, v67
	v_fmac_f32_e32 v68, v69, v66
	v_fma_f32 v65, -v65, v68, v67
	v_div_fmas_f32 v65, v65, v66, v68
	v_div_fixup_f32 v64, v65, v64, 1.0
	v_lshl_add_u32 v65, v100, 2, s10
	ds_write_b32 v65, v64 offset:8832
	v_add_f32_e32 v80, v60, v56
	v_add_f32_e32 v81, v52, v48
	v_add_f32_e32 v64, v80, v81
	v_add_f32_e32 v82, v61, v57
	v_add_f32_e32 v83, v53, v49
	v_add_f32_e32 v65, v82, v83
	v_add_f32_e32 v80, v62, v58
	v_add_f32_e32 v81, v54, v50
	v_add_f32_e32 v66, v80, v81
	v_add_f32_e32 v82, v63, v59
	v_add_f32_e32 v83, v55, v51
	v_add_f32_e32 v67, v82, v83
	v_add_f32_e32 v80, v44, v40
	v_add_f32_e32 v81, v36, v32
	v_add_f32_e32 v68, v80, v81
	v_add_f32_e32 v82, v45, v41
	v_add_f32_e32 v83, v37, v33
	v_add_f32_e32 v69, v82, v83
	v_add_f32_e32 v80, v46, v42
	v_add_f32_e32 v81, v38, v34
	v_add_f32_e32 v70, v80, v81
	v_add_f32_e32 v82, v47, v43
	v_add_f32_e32 v83, v39, v35
	v_add_f32_e32 v71, v82, v83
	v_add_f32_e32 v80, v28, v24
	v_add_f32_e32 v81, v20, v16
	v_add_f32_e32 v72, v80, v81
	v_add_f32_e32 v82, v29, v25
	v_add_f32_e32 v83, v21, v17
	v_add_f32_e32 v73, v82, v83
	v_add_f32_e32 v80, v30, v26
	v_add_f32_e32 v81, v22, v18
	v_add_f32_e32 v74, v80, v81
	v_add_f32_e32 v82, v31, v27
	v_add_f32_e32 v83, v23, v19
	v_add_f32_e32 v75, v82, v83
	v_add_f32_e32 v80, v12, v8
	v_add_f32_e32 v81, v4, v0
	v_add_f32_e32 v76, v80, v81
	v_add_f32_e32 v82, v13, v9
	v_add_f32_e32 v83, v5, v1
	v_add_f32_e32 v77, v82, v83
	v_add_f32_e32 v80, v14, v10
	v_add_f32_e32 v81, v6, v2
	v_add_f32_e32 v78, v80, v81
	v_add_f32_e32 v82, v15, v11
	v_add_f32_e32 v83, v7, v3
	v_add_f32_e32 v79, v82, v83
	v_add_f32_dpp v84, v64, v64 row_ror:8 row_mask:0xf bank_mask:0x3
	v_add_f32_dpp v84, v72, v72 row_ror:8 row_mask:0xf bank_mask:0xc
	v_add_f32_dpp v85, v65, v65 row_ror:8 row_mask:0xf bank_mask:0x3
	v_add_f32_dpp v85, v73, v73 row_ror:8 row_mask:0xf bank_mask:0xc
	v_add_f32_dpp v86, v66, v66 row_ror:8 row_mask:0xf bank_mask:0x3
	v_add_f32_dpp v86, v74, v74 row_ror:8 row_mask:0xf bank_mask:0xc
	v_add_f32_dpp v87, v67, v67 row_ror:8 row_mask:0xf bank_mask:0x3
	v_add_f32_dpp v87, v75, v75 row_ror:8 row_mask:0xf bank_mask:0xc
	v_add_f32_dpp v88, v68, v68 row_ror:8 row_mask:0xf bank_mask:0x3
	v_add_f32_dpp v88, v76, v76 row_ror:8 row_mask:0xf bank_mask:0xc
	v_add_f32_dpp v89, v69, v69 row_ror:8 row_mask:0xf bank_mask:0x3
	v_add_f32_dpp v89, v77, v77 row_ror:8 row_mask:0xf bank_mask:0xc
	v_add_f32_dpp v90, v70, v70 row_ror:8 row_mask:0xf bank_mask:0x3
	v_add_f32_dpp v90, v78, v78 row_ror:8 row_mask:0xf bank_mask:0xc
	v_add_f32_dpp v91, v71, v71 row_ror:8 row_mask:0xf bank_mask:0x3
	v_add_f32_dpp v91, v79, v79 row_ror:8 row_mask:0xf bank_mask:0xc
	v_add_f32_dpp v92, v84, v84 row_ror:12 row_mask:0xf bank_mask:0x5
	v_add_f32_dpp v92, v88, v88 row_ror:4 row_mask:0xf bank_mask:0xa
	v_add_f32_dpp v93, v85, v85 row_ror:12 row_mask:0xf bank_mask:0x5
	v_add_f32_dpp v93, v89, v89 row_ror:4 row_mask:0xf bank_mask:0xa
	v_add_f32_dpp v94, v86, v86 row_ror:12 row_mask:0xf bank_mask:0x5
	v_add_f32_dpp v94, v90, v90 row_ror:4 row_mask:0xf bank_mask:0xa
	v_add_f32_dpp v95, v87, v87 row_ror:12 row_mask:0xf bank_mask:0x5
	v_add_f32_dpp v95, v91, v91 row_ror:4 row_mask:0xf bank_mask:0xa
	v_add_f32_dpp v92, v92, v92 quad_perm:[2,3,0,1] row_mask:0xf bank_mask:0xf
	v_add_f32_dpp v93, v93, v93 quad_perm:[2,3,0,1] row_mask:0xf bank_mask:0xf
	v_add_f32_dpp v94, v94, v94 quad_perm:[2,3,0,1] row_mask:0xf bank_mask:0xf
	v_add_f32_dpp v95, v95, v95 quad_perm:[2,3,0,1] row_mask:0xf bank_mask:0xf
	v_add_f32_dpp v92, v92, v92 quad_perm:[1,0,3,2] row_mask:0xf bank_mask:0xf
	v_add_f32_dpp v93, v93, v93 quad_perm:[1,0,3,2] row_mask:0xf bank_mask:0xf
	v_add_f32_dpp v94, v94, v94 quad_perm:[1,0,3,2] row_mask:0xf bank_mask:0xf
	v_add_f32_dpp v95, v95, v95 quad_perm:[1,0,3,2] row_mask:0xf bank_mask:0xf
	v_mul_f32_e32 v92, 0x3c800000, v92
	v_mul_f32_e32 v93, 0x3c800000, v93
	v_mul_f32_e32 v94, 0x3c800000, v94
	v_mul_f32_e32 v95, 0x3c800000, v95
	v_max_f32_e32 v92, 0, v92
	v_max_f32_e32 v93, 0, v93
	v_max_f32_e32 v94, 0, v94
	v_max_f32_e32 v95, 0, v95
	v_add_f32_e32 v92, 0x3a83126f, v92
	v_add_f32_e32 v93, 0x3a83126f, v93
	v_add_f32_e32 v94, 0x3a83126f, v94
	v_add_f32_e32 v95, 0x3a83126f, v95
	v_add_f32_e32 v96, v92, v93
	v_add_f32_e32 v96, v96, v94
	v_add_f32_e32 v96, v96, v95
	v_add_f32_dpp v96, v92, v96 row_ror:12 row_mask:0xf bank_mask:0xf
	v_add_f32_dpp v96, v93, v96 row_ror:12 row_mask:0xf bank_mask:0xf
	v_add_f32_dpp v96, v94, v96 row_ror:12 row_mask:0xf bank_mask:0xf
	v_add_f32_dpp v96, v95, v96 row_ror:12 row_mask:0xf bank_mask:0xf
	v_add_f32_dpp v96, v92, v96 row_ror:8 row_mask:0xf bank_mask:0xf
	v_add_f32_dpp v96, v93, v96 row_ror:8 row_mask:0xf bank_mask:0xf
	v_add_f32_dpp v96, v94, v96 row_ror:8 row_mask:0xf bank_mask:0xf
	v_add_f32_dpp v96, v95, v96 row_ror:8 row_mask:0xf bank_mask:0xf
	v_add_f32_dpp v96, v92, v96 row_ror:4 row_mask:0xf bank_mask:0xf
	v_add_f32_dpp v96, v93, v96 row_ror:4 row_mask:0xf bank_mask:0xf
	v_add_f32_dpp v96, v94, v96 row_ror:4 row_mask:0xf bank_mask:0xf
	v_add_f32_dpp v96, v95, v96 row_ror:4 row_mask:0xf bank_mask:0xf
	v_mov_b32_e32 v97, v96
	s_nop 1
	v_permlane16_swap_b32_e32 v96, v97
	v_add_f32_e32 v96, v96, v97
	v_mov_b32_e32 v97, v96
	s_nop 1
	v_permlane32_swap_b32_e32 v96, v97
	v_add_f32_e32 v96, v96, v97
	s_nop 0
	v_readfirstlane_b32 s2, v96
	v_and_b32_e32 v99, 3, v100
	v_lshlrev_b32_e32 v98, 4, v101
	v_mov_b32_e32 v80, s2
	v_div_scale_f32 v81, s[2:3], v80, v80, 1.0
	v_rcp_f32_e32 v82, v81
	v_div_scale_f32 v83, vcc, 1.0, v80, 1.0
	v_fma_f32 v84, -v81, v82, 1.0
	v_fmac_f32_e32 v82, v84, v82
	v_mul_f32_e32 v84, v83, v82
	v_fma_f32 v85, -v81, v84, v83
	v_fmac_f32_e32 v84, v85, v82
	v_fma_f32 v81, -v81, v84, v83
	v_div_fmas_f32 v81, v81, v82, v84
	v_div_fixup_f32 v80, v81, v80, 1.0
	v_mul_f32_e32 v92, v80, v92
	v_mul_f32_e32 v93, v80, v93
	v_mul_f32_e32 v94, v80, v94
	v_mul_f32_e32 v95, v80, v95
	v_and_b32_e32 v97, 48, v100
	v_add3_u32 v98, v98, v97, s8
	v_cmp_eq_u32_e32 vcc, 0, v99
	s_and_saveexec_b64 s[2:3], vcc
	ds_write_b128 v98, v[92:95] offset:5632
	s_mov_b64 exec, s[2:3]
	v_add_f32_e32 v64, v60, v61
	v_add_f32_e32 v65, v62, v63
	v_add_f32_e32 v64, v64, v65
	v_add_f32_e32 v65, v44, v45
	v_add_f32_e32 v66, v46, v47
	v_add_f32_e32 v64, 0, v64
	v_add_f32_e32 v65, v65, v66
	v_add_f32_e32 v64, v64, v65
	v_add_f32_e32 v65, v28, v29
	v_add_f32_e32 v66, v30, v31
	v_add_f32_e32 v65, v65, v66
	v_add_f32_e32 v64, v64, v65
	v_add_f32_e32 v65, v12, v13
	v_add_f32_e32 v66, v14, v15
	v_add_f32_e32 v65, v65, v66
	v_add_f32_e32 v64, v64, v65
	v_mov_b32_e32 v65, v64
	s_nop 1
	v_permlane16_swap_b32_e32 v64, v65
	v_add_f32_e32 v64, v64, v65
	v_mov_b32_e32 v65, v64
	s_nop 1
	v_permlane32_swap_b32_e32 v64, v65
	v_add_f32_e32 v64, v64, v65
	v_add_f32_e32 v65, v56, v57
	v_add_f32_e32 v66, v58, v59
	v_add_f32_e32 v65, v65, v66
	v_add_f32_e32 v66, v40, v41
	v_add_f32_e32 v67, v42, v43
	v_add_f32_e32 v65, 0, v65
	v_add_f32_e32 v66, v66, v67
	v_add_f32_e32 v65, v65, v66
	v_add_f32_e32 v66, v24, v25
	v_add_f32_e32 v67, v26, v27
	v_add_f32_e32 v66, v66, v67
	v_add_f32_e32 v65, v65, v66
	v_add_f32_e32 v66, v8, v9
	v_add_f32_e32 v67, v10, v11
	v_add_f32_e32 v66, v66, v67
	v_add_f32_e32 v65, v65, v66
	v_mov_b32_e32 v66, v65
	s_nop 1
	v_permlane16_swap_b32_e32 v65, v66
	v_add_f32_e32 v65, v65, v66
	v_mov_b32_e32 v66, v65
	s_nop 1
	v_permlane32_swap_b32_e32 v65, v66
	v_add_f32_e32 v65, v65, v66
	v_add_f32_e32 v66, v52, v53
	v_add_f32_e32 v68, v54, v55
	v_add_f32_e32 v66, v66, v68
	v_add_f32_e32 v68, v36, v37
	v_add_f32_e32 v69, v38, v39
	v_add_f32_e32 v66, 0, v66
	v_add_f32_e32 v68, v68, v69
	v_add_f32_e32 v66, v66, v68
	v_add_f32_e32 v68, v20, v21
	v_add_f32_e32 v69, v22, v23
	v_add_f32_e32 v68, v68, v69
	v_add_f32_e32 v66, v66, v68
	v_add_f32_e32 v68, v4, v5
	v_add_f32_e32 v69, v6, v7
	v_add_f32_e32 v68, v68, v69
	v_add_f32_e32 v66, v66, v68
	v_mov_b32_e32 v68, v66
	s_nop 1
	v_permlane16_swap_b32_e32 v66, v68
	v_add_f32_e32 v66, v66, v68
	v_mov_b32_e32 v68, v66
	s_nop 1
	v_permlane32_swap_b32_e32 v66, v68
	v_mul_f32_e32 v64, 0x3c800000, v64
	v_mul_f32_e32 v65, 0x3c800000, v65
	v_add_f32_e32 v66, v66, v68
	v_max_f32_e32 v64, 0, v64
	v_max_f32_e32 v65, 0, v65
	v_mul_f32_e32 v66, 0x3c800000, v66
	v_add_f32_e32 v64, 0x3a83126f, v64
	v_add_f32_e32 v65, 0x3a83126f, v65
	v_max_f32_e32 v66, 0, v66
	v_add_f32_e32 v67, v64, v65
	v_add_f32_e32 v66, 0x3a83126f, v66
	v_add_f32_e32 v68, v67, v66
	v_add_f32_e32 v67, v48, v49
	v_add_f32_e32 v69, v50, v51
	v_add_f32_e32 v67, v67, v69
	v_add_f32_e32 v69, v32, v33
	v_add_f32_e32 v70, v34, v35
	v_add_f32_e32 v67, 0, v67
	v_add_f32_e32 v69, v69, v70
	v_add_f32_e32 v67, v67, v69
	v_add_f32_e32 v69, v16, v17
	v_add_f32_e32 v70, v18, v19
	v_add_f32_e32 v69, v69, v70
	v_add_f32_e32 v67, v67, v69
	v_add_f32_e32 v69, v0, v1
	v_add_f32_e32 v70, v2, v3
	v_add_f32_e32 v69, v69, v70
	v_add_f32_e32 v67, v67, v69
	v_mov_b32_e32 v69, v67
	s_nop 1
	v_permlane16_swap_b32_e32 v67, v69
	v_add_f32_e32 v67, v67, v69
	v_mov_b32_e32 v69, v67
	s_nop 1
	v_permlane32_swap_b32_e32 v67, v69
	v_add_f32_e32 v67, v67, v69
	v_mul_f32_e32 v67, 0x3c800000, v67
	v_max_f32_e32 v67, 0, v67
	v_add_f32_e32 v67, 0x3a83126f, v67
	v_add_f32_e32 v68, v68, v67
	s_mov_b32 s9, 0
	v_cmp_gt_u32_e64 s[0:1], 16, v100
	v_add_f32_dpp v68, v68, v68 row_ror:8 row_mask:0xf bank_mask:0xf bound_ctrl:1
	v_lshl_add_u32 v102, v100, 2, s8
	s_nop 0
	v_add_f32_dpp v68, v68, v68 row_ror:4 row_mask:0xf bank_mask:0xf bound_ctrl:1
	s_nop 1
	v_add_f32_dpp v68, v68, v68 row_ror:2 row_mask:0xf bank_mask:0xf bound_ctrl:1
	s_nop 1
	v_mov_b32_dpp v69, v68 row_ror:1 row_mask:0xf bank_mask:0xf bound_ctrl:1
	s_and_saveexec_b64 s[2:3], s[0:1]
	s_cbranch_execz .LBB1_36
	v_add_f32_e32 v68, v68, v69
	v_div_scale_f32 v69, s[4:5], v68, v68, 1.0
	v_rcp_f32_e32 v70, v69
	v_div_scale_f32 v71, vcc, 1.0, v68, 1.0
	v_fma_f32 v72, -v69, v70, 1.0
	v_fmac_f32_e32 v70, v72, v70
	v_mul_f32_e32 v72, v71, v70
	v_fma_f32 v73, -v69, v72, v71
	v_fmac_f32_e32 v72, v73, v70
	v_fma_f32 v69, -v69, v72, v71
	v_div_fmas_f32 v69, v69, v70, v72
	v_div_fixup_f32 v68, v69, v68, 1.0
	v_mul_f32_e32 v64, v68, v64
	v_mul_f32_e32 v65, v68, v65
	v_add_u32_e32 v69, 0x1400, v102
	ds_write2_b32 v69, v64, v65 offset0:192 offset1:208
	v_mul_f32_e32 v64, v68, v66
	v_mul_f32_e32 v65, v68, v67
	ds_write2_b32 v69, v64, v65 offset0:224 offset1:240
